# code placement: every loop after the hcat phase shifted by 4 bytes (8-byte phase of the GEMM loops flipped)
# speedup vs baseline: 1.0094x; 1.0015x over previous
.LBB0_155:
	s_nop 0
	v_writelane_b32 v238, s98, 0
	v_readlane_b32 s98, v235, 0
	v_readlane_b32 s99, v235, 1
	s_lshl_b32 s101, s26, 2
	v_add_u32_e32 v200, s33, v186
	v_mov_b32_e32 v201, s101
	s_load_dwordx2 s[100:101], s[46:47], 0x28
	v_mov_b32_e32 v207, 0x2aaaaaab
	v_lshlrev_b32_e32 v202, 2, v200
	v_cmp_gt_u32_e32 vcc, 0x12000, v202
	s_and_b64 exec, exec, vcc
	s_cbranch_execz .Lmodfin_end
	s_waitcnt lgkmcnt(0)
